# w13 int8 strip units: all 32 row loads of a unit issued up front (chunks 2,3 into fresh registers), counted vmcnt waits re-derived
# speedup vs baseline: 1.0014x; 1.0014x over previous
.LBB0_231:
	v_mov_b32_e32 v6, v0
	s_lshl_b32 s20, s20, 5
	v_ashrrev_i32_e32 v2, 31, v6
	v_lshrrev_b32_e32 v2, 29, v2
	s_and_b32 s20, s20, 0xffe0
	v_add_u32_e32 v2, v6, v2
	s_add_i32 s24, s20, 0xffffea00
	v_ashrrev_i32_e32 v3, 3, v2
	v_and_b32_e32 v2, -8, v2
	s_and_b64 s[4:5], s[4:5], exec
	v_sub_u32_e32 v57, v6, v2
	s_cselect_b32 s20, s20, s24
	v_lshlrev_b32_e32 v4, 2, v57
	v_add_u32_e32 v50, s20, v4
	v_lshlrev_b32_e32 v58, 2, v3
	v_mov_b64_e32 v[2:3], s[10:11]
	s_movk_i32 s4, 0x5800
	v_mad_i64_i32 v[2:3], s[4:5], v58, s4, v[2:3]
	v_max_i32_e32 v10, 0, v50
	v_lshl_add_u64 v[2:3], v[10:11], 2, v[2:3]
	s_movk_i32 s4, 0x5000
	v_add_co_u32_e32 v8, vcc, s4, v2
	s_mov_b32 s4, 0xb000
	s_nop 0
	v_addc_co_u32_e32 v9, vcc, 0, v3, vcc
	global_load_dwordx4 v[12:15], v[2:3], off
	global_load_dwordx4 v[16:19], v[8:9], off offset:2048
	v_add_co_u32_e32 v8, vcc, s4, v2
	s_mov_b32 s4, 0x580000
	s_nop 0
	v_addc_co_u32_e32 v9, vcc, 0, v3, vcc
	v_add_co_u32_e32 v24, vcc, s67, v2
	s_nop 1
	v_addc_co_u32_e32 v25, vcc, 0, v3, vcc
	global_load_dwordx4 v[20:23], v[8:9], off
	s_nop 0
	global_load_dwordx4 v[24:27], v[24:25], off offset:2048
	v_add_co_u32_e32 v8, vcc, s4, v2
	s_mov_b32 s4, 0x585000
	s_nop 0
	v_addc_co_u32_e32 v9, vcc, 0, v3, vcc
	v_add_co_u32_e32 v32, vcc, s4, v2
	s_mov_b32 s4, 0x58b000
	s_nop 0
	v_addc_co_u32_e32 v33, vcc, 0, v3, vcc
	global_load_dwordx4 v[28:31], v[8:9], off
	s_nop 0
	global_load_dwordx4 v[32:35], v[32:33], off offset:2048
	v_add_co_u32_e32 v8, vcc, s4, v2
	s_mov_b32 s4, 0x590000
	s_nop 0
	v_addc_co_u32_e32 v9, vcc, 0, v3, vcc
	v_add_co_u32_e32 v40, vcc, s4, v2
	s_mov_b32 s4, 0xb00000
	s_nop 0
	v_addc_co_u32_e32 v41, vcc, 0, v3, vcc
	global_load_dwordx4 v[36:39], v[8:9], off
	s_nop 0
	global_load_dwordx4 v[40:43], v[40:41], off offset:2048
	v_add_co_u32_e32 v8, vcc, s4, v2
	s_mov_b32 s4, 0xb05000
	s_nop 0
	v_addc_co_u32_e32 v9, vcc, 0, v3, vcc
	v_add_co_u32_e32 v48, vcc, s4, v2
	s_mov_b32 s4, 0xb0b000
	s_nop 0
	v_addc_co_u32_e32 v49, vcc, 0, v3, vcc
	global_load_dwordx4 v[44:47], v[8:9], off
	global_load_dwordx4 v[94:97], v[48:49], off offset:2048
	v_add_co_u32_e32 v8, vcc, s4, v2
	s_mov_b32 s4, 0xb10000
	s_nop 0
	v_addc_co_u32_e32 v9, vcc, 0, v3, vcc
	v_add_co_u32_e32 v48, vcc, s4, v2
	s_mov_b32 s4, 0x1080000
	s_nop 0
	v_addc_co_u32_e32 v49, vcc, 0, v3, vcc
	global_load_dwordx4 v[98:101], v[8:9], off
	global_load_dwordx4 v[102:105], v[48:49], off offset:2048
	v_add_co_u32_e32 v8, vcc, s4, v2
	s_mov_b32 s4, 0x1085000
	s_nop 0
	v_addc_co_u32_e32 v9, vcc, 0, v3, vcc
	v_add_co_u32_e32 v48, vcc, s4, v2
	s_mov_b32 s4, 0x108b000
	s_nop 0
	v_addc_co_u32_e32 v49, vcc, 0, v3, vcc
	global_load_dwordx4 v[106:109], v[8:9], off
	global_load_dwordx4 v[110:113], v[48:49], off offset:2048
	v_add_co_u32_e32 v8, vcc, s4, v2
	s_mov_b32 s4, 0x1090000
	s_nop 0
	v_addc_co_u32_e32 v9, vcc, 0, v3, vcc
	v_add_co_u32_e32 v48, vcc, s4, v2
	s_nop 1
	v_addc_co_u32_e32 v49, vcc, 0, v3, vcc
	global_load_dwordx4 v[114:117], v[8:9], off
	global_load_dwordx4 v[118:121], v[48:49], off offset:2048
	v_add_co_u32_e32 v244, vcc, 0x1600000, v2
	s_nop 1
	v_addc_co_u32_e32 v245, vcc, 0, v3, vcc
	global_load_dwordx4 v[180:183], v[244:245], off
	v_add_co_u32_e32 v244, vcc, 0x1605000, v2
	s_nop 1
	v_addc_co_u32_e32 v245, vcc, 0, v3, vcc
	global_load_dwordx4 v[184:187], v[244:245], off offset:2048
	v_add_co_u32_e32 v244, vcc, 0x160b000, v2
	s_nop 1
	v_addc_co_u32_e32 v245, vcc, 0, v3, vcc
	global_load_dwordx4 v[188:191], v[244:245], off
	v_add_co_u32_e32 v244, vcc, 0x1610000, v2
	s_nop 1
	v_addc_co_u32_e32 v245, vcc, 0, v3, vcc
	global_load_dwordx4 v[192:195], v[244:245], off offset:2048
	v_add_co_u32_e32 v244, vcc, 0x1b80000, v2
	s_nop 1
	v_addc_co_u32_e32 v245, vcc, 0, v3, vcc
	global_load_dwordx4 v[196:199], v[244:245], off
	v_add_co_u32_e32 v244, vcc, 0x1b85000, v2
	s_nop 1
	v_addc_co_u32_e32 v245, vcc, 0, v3, vcc
	global_load_dwordx4 v[200:203], v[244:245], off offset:2048
	v_add_co_u32_e32 v244, vcc, 0x1b8b000, v2
	s_nop 1
	v_addc_co_u32_e32 v245, vcc, 0, v3, vcc
	global_load_dwordx4 v[204:207], v[244:245], off
	v_add_co_u32_e32 v244, vcc, 0x1b90000, v2
	s_nop 1
	v_addc_co_u32_e32 v245, vcc, 0, v3, vcc
	global_load_dwordx4 v[208:211], v[244:245], off offset:2048
	v_add_co_u32_e32 v244, vcc, 0x2100000, v2
	s_nop 1
	v_addc_co_u32_e32 v245, vcc, 0, v3, vcc
	global_load_dwordx4 v[212:215], v[244:245], off
	v_add_co_u32_e32 v244, vcc, 0x2105000, v2
	s_nop 1
	v_addc_co_u32_e32 v245, vcc, 0, v3, vcc
	global_load_dwordx4 v[216:219], v[244:245], off offset:2048
	v_add_co_u32_e32 v244, vcc, 0x210b000, v2
	s_nop 1
	v_addc_co_u32_e32 v245, vcc, 0, v3, vcc
	global_load_dwordx4 v[220:223], v[244:245], off
	v_add_co_u32_e32 v244, vcc, 0x2110000, v2
	s_nop 1
	v_addc_co_u32_e32 v245, vcc, 0, v3, vcc
	global_load_dwordx4 v[224:227], v[244:245], off offset:2048
	v_add_co_u32_e32 v244, vcc, 0x2680000, v2
	s_nop 1
	v_addc_co_u32_e32 v245, vcc, 0, v3, vcc
	global_load_dwordx4 v[228:231], v[244:245], off
	v_add_co_u32_e32 v244, vcc, 0x2685000, v2
	s_nop 1
	v_addc_co_u32_e32 v245, vcc, 0, v3, vcc
	global_load_dwordx4 v[232:235], v[244:245], off offset:2048
	v_add_co_u32_e32 v244, vcc, 0x268b000, v2
	s_nop 1
	v_addc_co_u32_e32 v245, vcc, 0, v3, vcc
	global_load_dwordx4 v[236:239], v[244:245], off
	v_add_co_u32_e32 v244, vcc, 0x2690000, v2
	s_nop 1
	v_addc_co_u32_e32 v245, vcc, 0, v3, vcc
	global_load_dwordx4 v[240:243], v[244:245], off offset:2048
	v_cmp_gt_i32_e32 vcc, 0, v50
	s_waitcnt vmcnt(31)
	s_nop 0
	v_cndmask_b32_e64 v5, v14, 0, vcc
	v_cndmask_b32_e64 v7, v15, 0, vcc
	v_cndmask_b32_e64 v8, v12, 0, vcc
	v_cndmask_b32_e64 v9, v13, 0, vcc
	s_waitcnt vmcnt(30)
	v_cndmask_b32_e64 v10, v18, 0, vcc
	v_cndmask_b32_e64 v12, v19, 0, vcc
	v_cndmask_b32_e64 v13, v16, 0, vcc
	v_cndmask_b32_e64 v14, v17, 0, vcc
	v_cvt_pk_bf16_f32 v71, v8, v9
	v_cvt_pk_bf16_f32 v67, v5, v7
	v_cvt_pk_bf16_f32 v72, v13, v14
	v_cvt_pk_bf16_f32 v68, v10, v12
	v_max3_f32 v8, |v8|, 0, |v13|
	v_max3_f32 v9, |v9|, 0, |v14|
	v_max3_f32 v5, |v5|, 0, |v10|
	v_max3_f32 v7, |v7|, 0, |v12|
	s_waitcnt vmcnt(29)
	v_cndmask_b32_e64 v10, v22, 0, vcc
	v_cndmask_b32_e64 v12, v23, 0, vcc
	v_cndmask_b32_e64 v13, v20, 0, vcc
	v_cndmask_b32_e64 v14, v21, 0, vcc
	s_waitcnt vmcnt(28)
	v_cndmask_b32_e64 v15, v26, 0, vcc
	v_cndmask_b32_e64 v16, v27, 0, vcc
	v_cndmask_b32_e64 v17, v24, 0, vcc
	v_cndmask_b32_e64 v18, v25, 0, vcc
	v_cvt_pk_bf16_f32 v73, v13, v14
	v_cvt_pk_bf16_f32 v69, v10, v12
	v_cvt_pk_bf16_f32 v74, v17, v18
	v_cvt_pk_bf16_f32 v70, v15, v16
	v_max3_f32 v7, v7, |v12|, |v16|
	v_max3_f32 v5, v5, |v10|, |v15|
	v_max3_f32 v9, v9, |v14|, |v18|
	v_max3_f32 v8, v8, |v13|, |v17|
	s_waitcnt vmcnt(27)
	v_cndmask_b32_e64 v10, v30, 0, vcc
	v_cndmask_b32_e64 v12, v31, 0, vcc
	v_cndmask_b32_e64 v13, v28, 0, vcc
	v_cndmask_b32_e64 v14, v29, 0, vcc
	s_waitcnt vmcnt(26)
	v_cndmask_b32_e64 v15, v34, 0, vcc
	v_cndmask_b32_e64 v16, v35, 0, vcc
	v_cndmask_b32_e64 v17, v32, 0, vcc
	v_cndmask_b32_e64 v18, v33, 0, vcc
	v_cvt_pk_bf16_f32 v63, v13, v14
	v_cvt_pk_bf16_f32 v53, v10, v12
	v_cvt_pk_bf16_f32 v64, v17, v18
	v_cvt_pk_bf16_f32 v54, v15, v16
	v_max3_f32 v8, v8, |v13|, |v17|
	v_max3_f32 v9, v9, |v14|, |v18|
	v_max3_f32 v5, v5, |v10|, |v15|
	v_max3_f32 v7, v7, |v12|, |v16|
	s_waitcnt vmcnt(25)
	v_cndmask_b32_e64 v10, v38, 0, vcc
	v_cndmask_b32_e64 v12, v39, 0, vcc
	v_cndmask_b32_e64 v13, v36, 0, vcc
	v_cndmask_b32_e64 v14, v37, 0, vcc
	s_waitcnt vmcnt(24)
	v_cndmask_b32_e64 v15, v42, 0, vcc
	v_cndmask_b32_e64 v16, v43, 0, vcc
	v_cndmask_b32_e64 v17, v40, 0, vcc
	v_cndmask_b32_e64 v18, v41, 0, vcc
	v_cvt_pk_bf16_f32 v65, v13, v14
	v_cvt_pk_bf16_f32 v55, v10, v12
	v_max3_f32 v7, v7, |v12|, |v16|
	v_max3_f32 v5, v5, |v10|, |v15|
	v_max3_f32 v10, v9, |v14|, |v18|
	v_max3_f32 v34, v8, |v13|, |v17|
	v_cvt_pk_bf16_f32 v66, v17, v18
	v_cvt_pk_bf16_f32 v56, v15, v16
	s_waitcnt vmcnt(23)
	v_cndmask_b32_e64 v8, v46, 0, vcc
	v_cndmask_b32_e64 v9, v47, 0, vcc
	v_cndmask_b32_e64 v32, v44, 0, vcc
	v_cndmask_b32_e64 v33, v45, 0, vcc
	s_waitcnt vmcnt(22)
	v_cndmask_b32_e64 v35, v96, 0, vcc
	v_cndmask_b32_e64 v36, v97, 0, vcc
	v_cndmask_b32_e64 v37, v94, 0, vcc
	v_cndmask_b32_e64 v38, v95, 0, vcc
	v_cvt_pk_bf16_f32 v59, v32, v33
	v_cvt_pk_bf16_f32 v48, v8, v9
	v_cvt_pk_bf16_f32 v60, v37, v38
	v_cvt_pk_bf16_f32 v49, v35, v36
	v_max3_f32 v32, v34, |v32|, |v37|
	v_max3_f32 v10, v10, |v33|, |v38|
	v_max3_f32 v5, v5, |v8|, |v35|
	v_max3_f32 v7, v7, |v9|, |v36|
	s_waitcnt vmcnt(21)
	v_cndmask_b32_e64 v8, v100, 0, vcc
	v_cndmask_b32_e64 v9, v101, 0, vcc
	v_cndmask_b32_e64 v33, v98, 0, vcc
	v_cndmask_b32_e64 v34, v99, 0, vcc
	s_waitcnt vmcnt(20)
	v_cndmask_b32_e64 v35, v104, 0, vcc
	v_cndmask_b32_e64 v36, v105, 0, vcc
	v_cndmask_b32_e64 v37, v102, 0, vcc
	v_cndmask_b32_e64 v38, v103, 0, vcc
	v_cvt_pk_bf16_f32 v61, v33, v34
	v_cvt_pk_bf16_f32 v51, v8, v9
	v_cvt_pk_bf16_f32 v62, v37, v38
	v_cvt_pk_bf16_f32 v52, v35, v36
	v_max3_f32 v7, v7, |v9|, |v36|
	v_max3_f32 v5, v5, |v8|, |v35|
	v_max3_f32 v8, v10, |v34|, |v38|
	v_max3_f32 v9, v32, |v33|, |v37|
	s_waitcnt vmcnt(19)
	v_cndmask_b32_e64 v10, v108, 0, vcc
	v_cndmask_b32_e64 v32, v109, 0, vcc
	v_cndmask_b32_e64 v33, v106, 0, vcc
	v_cndmask_b32_e64 v34, v107, 0, vcc
	s_waitcnt vmcnt(18)
	v_cndmask_b32_e64 v35, v112, 0, vcc
	v_cndmask_b32_e64 v38, v113, 0, vcc
	v_cndmask_b32_e64 v39, v110, 0, vcc
	v_cndmask_b32_e64 v40, v111, 0, vcc
	v_cvt_pk_bf16_f32 v44, v33, v34
	v_cvt_pk_bf16_f32 v36, v10, v32
	v_cvt_pk_bf16_f32 v45, v39, v40
	v_cvt_pk_bf16_f32 v37, v35, v38
	v_max3_f32 v9, v9, |v33|, |v39|
	v_max3_f32 v8, v8, |v34|, |v40|
	v_max3_f32 v5, v5, |v10|, |v35|
	v_max3_f32 v7, v7, |v32|, |v38|
	s_waitcnt vmcnt(17)
	v_cndmask_b32_e64 v10, v116, 0, vcc
	v_cndmask_b32_e64 v32, v117, 0, vcc
	v_cndmask_b32_e64 v33, v114, 0, vcc
	v_cndmask_b32_e64 v34, v115, 0, vcc
	s_waitcnt vmcnt(16)
	v_cndmask_b32_e64 v35, v120, 0, vcc
	v_cndmask_b32_e64 v40, v121, 0, vcc
	v_cndmask_b32_e64 v41, v118, 0, vcc
	v_cndmask_b32_e64 v42, v119, 0, vcc
	v_cvt_pk_bf16_f32 v46, v33, v34
	v_cvt_pk_bf16_f32 v38, v10, v32
	v_max3_f32 v7, v7, |v32|, |v40|
	v_max3_f32 v5, v5, |v10|, |v35|
	v_max3_f32 v10, v8, |v34|, |v42|
	v_max3_f32 v34, v9, |v33|, |v41|
	v_cvt_pk_bf16_f32 v47, v41, v42
	v_cvt_pk_bf16_f32 v39, v35, v40
	s_waitcnt vmcnt(15)
	v_cndmask_b32_e64 v2, v182, 0, vcc
	v_cndmask_b32_e64 v3, v183, 0, vcc
	v_cndmask_b32_e64 v8, v180, 0, vcc
	v_cndmask_b32_e64 v9, v181, 0, vcc
	s_waitcnt vmcnt(14)
	v_cndmask_b32_e64 v12, v186, 0, vcc
	v_cndmask_b32_e64 v13, v187, 0, vcc
	v_cndmask_b32_e64 v14, v184, 0, vcc
	v_cndmask_b32_e64 v15, v185, 0, vcc
	v_cvt_pk_bf16_f32 v40, v8, v9
	v_cvt_pk_bf16_f32 v32, v2, v3
	v_cvt_pk_bf16_f32 v41, v14, v15
	v_cvt_pk_bf16_f32 v33, v12, v13
	v_max3_f32 v8, v34, |v8|, |v14|
	v_max3_f32 v9, v10, |v9|, |v15|
	v_max3_f32 v2, v5, |v2|, |v12|
	v_max3_f32 v3, v7, |v3|, |v13|
	s_waitcnt vmcnt(13)
	v_cndmask_b32_e64 v5, v190, 0, vcc
	v_cndmask_b32_e64 v7, v191, 0, vcc
	v_cndmask_b32_e64 v10, v188, 0, vcc
	v_cndmask_b32_e64 v12, v189, 0, vcc
	s_waitcnt vmcnt(12)
	v_cndmask_b32_e64 v13, v194, 0, vcc
	v_cndmask_b32_e64 v14, v195, 0, vcc
	v_cndmask_b32_e64 v15, v192, 0, vcc
	v_cndmask_b32_e64 v16, v193, 0, vcc
	v_cvt_pk_bf16_f32 v42, v10, v12
	v_cvt_pk_bf16_f32 v34, v5, v7
	v_cvt_pk_bf16_f32 v43, v15, v16
	v_cvt_pk_bf16_f32 v35, v13, v14
	v_max3_f32 v3, v3, |v7|, |v14|
	v_max3_f32 v2, v2, |v5|, |v13|
	v_max3_f32 v5, v9, |v12|, |v16|
	v_max3_f32 v7, v8, |v10|, |v15|
	s_waitcnt vmcnt(11)
	v_cndmask_b32_e64 v8, v198, 0, vcc
	v_cndmask_b32_e64 v9, v199, 0, vcc
	v_cndmask_b32_e64 v10, v196, 0, vcc
	v_cndmask_b32_e64 v12, v197, 0, vcc
	s_waitcnt vmcnt(10)
	v_cndmask_b32_e64 v13, v202, 0, vcc
	v_cndmask_b32_e64 v14, v203, 0, vcc
	v_cndmask_b32_e64 v15, v200, 0, vcc
	v_cndmask_b32_e64 v16, v201, 0, vcc
	v_cvt_pk_bf16_f32 v28, v10, v12
	v_cvt_pk_bf16_f32 v24, v8, v9
	v_cvt_pk_bf16_f32 v29, v15, v16
	v_cvt_pk_bf16_f32 v25, v13, v14
	v_max3_f32 v7, v7, |v10|, |v15|
	v_max3_f32 v5, v5, |v12|, |v16|
	v_max3_f32 v2, v2, |v8|, |v13|
	v_max3_f32 v3, v3, |v9|, |v14|
	s_waitcnt vmcnt(9)
	v_cndmask_b32_e64 v8, v206, 0, vcc
	v_cndmask_b32_e64 v9, v207, 0, vcc
	v_cndmask_b32_e64 v10, v204, 0, vcc
	v_cndmask_b32_e64 v12, v205, 0, vcc
	s_waitcnt vmcnt(8)
	v_cndmask_b32_e64 v13, v210, 0, vcc
	v_cndmask_b32_e64 v14, v211, 0, vcc
	v_cndmask_b32_e64 v15, v208, 0, vcc
	v_cndmask_b32_e64 v16, v209, 0, vcc
	v_max3_f32 v3, v3, |v9|, |v14|
	v_max3_f32 v2, v2, |v8|, |v13|
	v_max3_f32 v5, v5, |v12|, |v16|
	v_max3_f32 v7, v7, |v10|, |v15|
	v_cvt_pk_bf16_f32 v30, v10, v12
	v_cvt_pk_bf16_f32 v26, v8, v9
	v_cvt_pk_bf16_f32 v31, v15, v16
	v_cvt_pk_bf16_f32 v27, v13, v14
	s_waitcnt vmcnt(7)
	v_cndmask_b32_e64 v8, v214, 0, vcc
	v_cndmask_b32_e64 v9, v215, 0, vcc
	v_cndmask_b32_e64 v10, v212, 0, vcc
	v_cndmask_b32_e64 v12, v213, 0, vcc
	s_waitcnt vmcnt(6)
	v_cndmask_b32_e64 v13, v218, 0, vcc
	v_cndmask_b32_e64 v14, v219, 0, vcc
	v_cndmask_b32_e64 v15, v216, 0, vcc
	v_cndmask_b32_e64 v18, v217, 0, vcc
	v_cvt_pk_bf16_f32 v20, v10, v12
	v_cvt_pk_bf16_f32 v16, v8, v9
	v_cvt_pk_bf16_f32 v21, v15, v18
	v_cvt_pk_bf16_f32 v17, v13, v14
	v_max3_f32 v7, v7, |v10|, |v15|
	v_max3_f32 v5, v5, |v12|, |v18|
	v_max3_f32 v2, v2, |v8|, |v13|
	v_max3_f32 v3, v3, |v9|, |v14|
	s_waitcnt vmcnt(5)
	v_cndmask_b32_e64 v8, v222, 0, vcc
	v_cndmask_b32_e64 v9, v223, 0, vcc
	v_cndmask_b32_e64 v10, v220, 0, vcc
	v_cndmask_b32_e64 v12, v221, 0, vcc
	s_waitcnt vmcnt(4)
	v_cndmask_b32_e64 v13, v226, 0, vcc
	v_cndmask_b32_e64 v14, v227, 0, vcc
	v_cndmask_b32_e64 v15, v224, 0, vcc
	v_cndmask_b32_e64 v75, v225, 0, vcc
	v_cvt_pk_bf16_f32 v22, v10, v12
	v_cvt_pk_bf16_f32 v18, v8, v9
	v_cvt_pk_bf16_f32 v23, v15, v75
	v_cvt_pk_bf16_f32 v19, v13, v14
	v_max3_f32 v3, v3, |v9|, |v14|
	v_max3_f32 v2, v2, |v8|, |v13|
	v_max3_f32 v5, v5, |v12|, |v75|
	v_max3_f32 v9, v7, |v10|, |v15|
	s_waitcnt vmcnt(3)
	v_cndmask_b32_e64 v10, v230, 0, vcc
	v_cndmask_b32_e64 v14, v231, 0, vcc
	v_cndmask_b32_e64 v15, v228, 0, vcc
	v_cndmask_b32_e64 v75, v229, 0, vcc
	s_waitcnt vmcnt(2)
	v_cndmask_b32_e64 v76, v234, 0, vcc
	v_cndmask_b32_e64 v77, v235, 0, vcc
	v_cndmask_b32_e64 v94, v232, 0, vcc
	v_cndmask_b32_e64 v95, v233, 0, vcc
	v_cvt_pk_bf16_f32 v12, v15, v75
	v_cvt_pk_bf16_f32 v7, v10, v14
	v_cvt_pk_bf16_f32 v13, v94, v95
	v_cvt_pk_bf16_f32 v8, v76, v77
	v_max3_f32 v94, v9, |v15|, |v94|
	v_max3_f32 v5, v5, |v75|, |v95|
	v_max3_f32 v2, v2, |v10|, |v76|
	v_max3_f32 v3, v3, |v14|, |v77|
	s_waitcnt vmcnt(1)
	v_cndmask_b32_e64 v75, v238, 0, vcc
	v_cndmask_b32_e64 v76, v239, 0, vcc
	v_cndmask_b32_e64 v77, v236, 0, vcc
	v_cndmask_b32_e64 v95, v237, 0, vcc
	s_waitcnt vmcnt(0)
	v_cndmask_b32_e64 v96, v242, 0, vcc
	v_cndmask_b32_e64 v97, v243, 0, vcc
	v_cndmask_b32_e64 v98, v240, 0, vcc
	v_cndmask_b32_e64 v99, v241, 0, vcc
	v_cvt_pk_bf16_f32 v14, v77, v95
	v_cvt_pk_bf16_f32 v9, v75, v76
	v_max3_f32 v76, v3, |v76|, |v97|
	v_max3_f32 v75, v2, |v75|, |v96|
	v_max3_f32 v2, v5, |v95|, |v99|
	v_max3_f32 v3, v94, |v77|, |v98|
	v_cvt_pk_bf16_f32 v15, v98, v99
	v_cvt_pk_bf16_f32 v10, v96, v97
	v_and_b32_e32 v96, 63, v6
	v_lshlrev_b32_e32 v5, 2, v96
	v_xor_b32_e32 v77, 32, v5
	ds_bpermute_b32 v94, v77, v3
	ds_bpermute_b32 v95, v77, v2
	v_xor_b32_e32 v97, 64, v5
	ds_bpermute_b32 v99, v77, v75
	ds_bpermute_b32 v77, v77, v76
	s_waitcnt lgkmcnt(3)
	v_max_f32_e32 v94, v94, v94
	s_waitcnt lgkmcnt(2)
	v_max_f32_e32 v95, v95, v95
	v_max_f32_e32 v3, v3, v94
	v_max_f32_e32 v94, v2, v95
	ds_bpermute_b32 v95, v97, v94
	v_xor_b32_e32 v98, 0x80, v5
	s_waitcnt lgkmcnt(1)
	v_max_f32_e32 v77, v77, v77
	v_max_f32_e32 v76, v76, v77
	ds_bpermute_b32 v2, v97, v3
	s_waitcnt lgkmcnt(1)
	v_max_f32_e32 v5, v95, v95
	v_max_f32_e32 v5, v94, v5
	v_max_f32_e32 v94, v99, v99
	v_max_f32_e32 v75, v75, v94
	ds_bpermute_b32 v94, v97, v75
	ds_bpermute_b32 v95, v97, v76
	s_waitcnt lgkmcnt(2)
	v_max_f32_e32 v2, v2, v2
	v_max_f32_e32 v2, v3, v2
	ds_bpermute_b32 v3, v98, v2
	s_waitcnt lgkmcnt(2)
	v_max_f32_e32 v94, v94, v94
	s_waitcnt lgkmcnt(1)
	v_max_f32_e32 v95, v95, v95
	v_max_f32_e32 v75, v75, v94
	v_max_f32_e32 v76, v76, v95
	ds_bpermute_b32 v77, v98, v5
	ds_bpermute_b32 v94, v98, v75
	ds_bpermute_b32 v95, v98, v76
	v_cmp_gt_u32_e32 vcc, 8, v96
	s_and_saveexec_b64 s[4:5], vcc
	s_cbranch_execz .LBB0_233
	s_waitcnt lgkmcnt(3)
	v_max_f32_e32 v3, v3, v3
	v_max_f32_e32 v2, v2, v2
	v_max_f32_e32 v96, v2, v3
	s_waitcnt lgkmcnt(2)
	v_max_f32_e32 v2, v77, v77
	v_max_f32_e32 v3, v5, v5
	v_max_f32_e32 v97, v3, v2
	s_waitcnt lgkmcnt(1)
	v_max_f32_e32 v2, v94, v94
	v_max_f32_e32 v3, v75, v75
	v_max_f32_e32 v98, v3, v2
	s_waitcnt lgkmcnt(0)
	v_max_f32_e32 v2, v95, v95
	v_max_f32_e32 v3, v76, v76
	v_max_f32_e32 v99, v3, v2
	v_lshrrev_b32_e32 v2, 3, v6
	v_and_b32_e32 v2, 0xffffff8, v2
	v_add_u32_e32 v2, v2, v57
	v_lshl_add_u32 v2, v2, 4, 0
	v_add_u32_e32 v2, 0x10200, v2
	ds_write_b128 v2, v[96:99]
